# baseline (speedup 1.0000x reference)
.LBB0_37:
	s_or_b64 exec, exec, s[14:15]
	v_readfirstlane_b32 s94, v0
	s_lshr_b32 s94, s94, 6
	s_cmp_lg_u32 s94, 1
	s_cbranch_scc1 .Llpt_done
	s_add_i32 s95, s33, 1
	s_ashr_i32 s95, s95, 1
	v_add_u32_e32 v100, 16, v3
	v_add_u32_e32 v101, 0x50, v3
	v_lshlrev_b32_e32 v102, 3, v100
	v_lshlrev_b32_e32 v103, 3, v101
	v_add_u32_e32 v102, 0x1dd00, v102
	v_add_u32_e32 v103, 0x1dd00, v103
	ds_read_b64 v[104:105], v102
	ds_read_b64 v[106:107], v103
	v_mov_b32_e32 v110, 0x26dd0
	s_waitcnt lgkmcnt(0)
	v_add_u32_e32 v104, v104, v105
	v_add_u32_e32 v106, v106, v107
	v_add_u32_e32 v104, 15, v104
	v_add_u32_e32 v106, 15, v106
	v_lshrrev_b32_e32 v104, 4, v104
	v_lshrrev_b32_e32 v106, 4, v106
	v_max_u32_e32 v104, 1, v104
	v_max_u32_e32 v106, 1, v106
	v_min_u32_e32 v104, 1, v104
	v_min_u32_e32 v106, 1, v106
	v_cmp_gt_i32_e32 vcc, s95, v100
	s_nop 1
	v_cndmask_b32_e32 v104, 0, v104, vcc
	v_cmp_gt_i32_e32 vcc, s95, v101
	s_nop 1
	v_cndmask_b32_e32 v106, 0, v106, vcc
	s_mov_b32 s94, 16
	v_cmp_eq_u32_e64 s[34:35], 7, v104
	v_cmp_eq_u32_e64 s[36:37], 7, v106
	s_bcnt1_i32_b64 s73, s[34:35]
	s_nop 0
	v_mbcnt_lo_u32_b32 v108, s34, 0
	v_mbcnt_hi_u32_b32 v108, s35, v108
	v_add_u32_e32 v108, s94, v108
	s_add_i32 s94, s94, s73
	v_mbcnt_lo_u32_b32 v109, s36, 0
	v_mbcnt_hi_u32_b32 v109, s37, v109
	v_add_u32_e32 v109, s94, v109
	s_bcnt1_i32_b64 s73, s[36:37]
	s_add_i32 s94, s94, s73
	v_lshl_add_u32 v108, v108, 2, v110
	v_lshl_add_u32 v109, v109, 2, v110
	s_mov_b64 exec, s[34:35]
	ds_write_b32 v108, v100
	s_mov_b64 exec, s[36:37]
	ds_write_b32 v109, v101
	s_mov_b64 exec, -1
	v_cmp_eq_u32_e64 s[34:35], 6, v104
	v_cmp_eq_u32_e64 s[36:37], 6, v106
	s_bcnt1_i32_b64 s73, s[34:35]
	s_nop 0
	v_mbcnt_lo_u32_b32 v108, s34, 0
	v_mbcnt_hi_u32_b32 v108, s35, v108
	v_add_u32_e32 v108, s94, v108
	s_add_i32 s94, s94, s73
	v_mbcnt_lo_u32_b32 v109, s36, 0
	v_mbcnt_hi_u32_b32 v109, s37, v109
	v_add_u32_e32 v109, s94, v109
	s_bcnt1_i32_b64 s73, s[36:37]
	s_add_i32 s94, s94, s73
	v_lshl_add_u32 v108, v108, 2, v110
	v_lshl_add_u32 v109, v109, 2, v110
	s_mov_b64 exec, s[34:35]
	ds_write_b32 v108, v100
	s_mov_b64 exec, s[36:37]
	ds_write_b32 v109, v101
	s_mov_b64 exec, -1
	v_cmp_eq_u32_e64 s[34:35], 5, v104
	v_cmp_eq_u32_e64 s[36:37], 5, v106
	s_bcnt1_i32_b64 s73, s[34:35]
	s_nop 0
	v_mbcnt_lo_u32_b32 v108, s34, 0
	v_mbcnt_hi_u32_b32 v108, s35, v108
	v_add_u32_e32 v108, s94, v108
	s_add_i32 s94, s94, s73
	v_mbcnt_lo_u32_b32 v109, s36, 0
	v_mbcnt_hi_u32_b32 v109, s37, v109
	v_add_u32_e32 v109, s94, v109
	s_bcnt1_i32_b64 s73, s[36:37]
	s_add_i32 s94, s94, s73
	v_lshl_add_u32 v108, v108, 2, v110
	v_lshl_add_u32 v109, v109, 2, v110
	s_mov_b64 exec, s[34:35]
	ds_write_b32 v108, v100
	s_mov_b64 exec, s[36:37]
	ds_write_b32 v109, v101
	s_mov_b64 exec, -1
	v_cmp_eq_u32_e64 s[34:35], 4, v104
	v_cmp_eq_u32_e64 s[36:37], 4, v106
	s_bcnt1_i32_b64 s73, s[34:35]
	s_nop 0
	v_mbcnt_lo_u32_b32 v108, s34, 0
	v_mbcnt_hi_u32_b32 v108, s35, v108
	v_add_u32_e32 v108, s94, v108
	s_add_i32 s94, s94, s73
	v_mbcnt_lo_u32_b32 v109, s36, 0
	v_mbcnt_hi_u32_b32 v109, s37, v109
	v_add_u32_e32 v109, s94, v109
	s_bcnt1_i32_b64 s73, s[36:37]
	s_add_i32 s94, s94, s73
	v_lshl_add_u32 v108, v108, 2, v110
	v_lshl_add_u32 v109, v109, 2, v110
	s_mov_b64 exec, s[34:35]
	ds_write_b32 v108, v100
	s_mov_b64 exec, s[36:37]
	ds_write_b32 v109, v101
	s_mov_b64 exec, -1
	v_cmp_eq_u32_e64 s[34:35], 3, v104
	v_cmp_eq_u32_e64 s[36:37], 3, v106
	s_bcnt1_i32_b64 s73, s[34:35]
	s_nop 0
	v_mbcnt_lo_u32_b32 v108, s34, 0
	v_mbcnt_hi_u32_b32 v108, s35, v108
	v_add_u32_e32 v108, s94, v108
	s_add_i32 s94, s94, s73
	v_mbcnt_lo_u32_b32 v109, s36, 0
	v_mbcnt_hi_u32_b32 v109, s37, v109
	v_add_u32_e32 v109, s94, v109
	s_bcnt1_i32_b64 s73, s[36:37]
	s_add_i32 s94, s94, s73
	v_lshl_add_u32 v108, v108, 2, v110
	v_lshl_add_u32 v109, v109, 2, v110
	s_mov_b64 exec, s[34:35]
	ds_write_b32 v108, v100
	s_mov_b64 exec, s[36:37]
	ds_write_b32 v109, v101
	s_mov_b64 exec, -1
	v_cmp_eq_u32_e64 s[34:35], 2, v104
	v_cmp_eq_u32_e64 s[36:37], 2, v106
	s_bcnt1_i32_b64 s73, s[34:35]
	s_nop 0
	v_mbcnt_lo_u32_b32 v108, s34, 0
	v_mbcnt_hi_u32_b32 v108, s35, v108
	v_add_u32_e32 v108, s94, v108
	s_add_i32 s94, s94, s73
	v_mbcnt_lo_u32_b32 v109, s36, 0
	v_mbcnt_hi_u32_b32 v109, s37, v109
	v_add_u32_e32 v109, s94, v109
	s_bcnt1_i32_b64 s73, s[36:37]
	s_add_i32 s94, s94, s73
	v_lshl_add_u32 v108, v108, 2, v110
	v_lshl_add_u32 v109, v109, 2, v110
	s_mov_b64 exec, s[34:35]
	ds_write_b32 v108, v100
	s_mov_b64 exec, s[36:37]
	ds_write_b32 v109, v101
	s_mov_b64 exec, -1
	v_cmp_eq_u32_e64 s[34:35], 1, v104
	v_cmp_eq_u32_e64 s[36:37], 1, v106
	s_bcnt1_i32_b64 s73, s[34:35]
	s_nop 0
	v_mbcnt_lo_u32_b32 v108, s34, 0
	v_mbcnt_hi_u32_b32 v108, s35, v108
	v_add_u32_e32 v108, s94, v108
	s_add_i32 s94, s94, s73
	v_mbcnt_lo_u32_b32 v109, s36, 0
	v_mbcnt_hi_u32_b32 v109, s37, v109
	v_add_u32_e32 v109, s94, v109
	s_bcnt1_i32_b64 s73, s[36:37]
	s_add_i32 s94, s94, s73
	v_lshl_add_u32 v108, v108, 2, v110
	v_lshl_add_u32 v109, v109, 2, v110
	s_mov_b64 exec, s[34:35]
	ds_write_b32 v108, v100
	s_mov_b64 exec, s[36:37]
	ds_write_b32 v109, v101
	s_mov_b64 exec, -1
